# seven 64-lane ds_bpermute xor-butterfly reductions in the norm / sum phases rewritten with DPP row ops + v_readlane (same add order, bitwise-identical result)
# speedup vs baseline: 1.0030x; 1.0030x over previous
.LBB0_390:
	s_waitcnt vmcnt(3)
	v_pk_mul_f32 v[96:97], v[64:65], v[64:65]
	v_pk_mul_f32 v[98:99], v[62:63], v[62:63]
	s_waitcnt vmcnt(2)
	v_pk_mul_f32 v[92:93], v[60:61], v[60:61]
	v_pk_mul_f32 v[94:95], v[58:59], v[58:59]
	v_pk_mov_b32 v[100:101], v[98:99], v[96:97] op_sel:[1,0]
	v_mov_b32_e32 v99, v97
	v_pk_add_f32 v[96:97], v[100:101], v[98:99]
	v_pk_mov_b32 v[98:99], v[94:95], v[92:93] op_sel:[1,0]
	v_mov_b32_e32 v95, v93
	v_pk_add_f32 v[92:93], v[98:99], v[94:95]
	v_pk_add_f32 v[96:97], v[96:97], v[96:97] op_sel_hi:[0,1]
	v_pk_add_f32 v[92:93], v[92:93], v[92:93] op_sel_hi:[0,1]
	s_waitcnt vmcnt(1)
	v_mul_f32_e32 v92, v54, v54
	v_pk_fma_f32 v[94:95], v[54:55], v[54:55], v[92:93] op_sel_hi:[1,1,0]
	v_mul_f32_e32 v92, v56, v56
	v_pk_fma_f32 v[98:99], v[56:57], v[56:57], v[92:93] op_sel_hi:[1,1,0]
	s_waitcnt vmcnt(0)
	v_mul_f32_e32 v94, v50, v50
	v_mul_f32_e32 v98, v51, v51
	v_mul_f32_e32 v96, v52, v52
	v_mul_f32_e32 v92, v53, v53
	v_pk_add_f32 v[94:95], v[94:95], v[98:99]
	v_pk_add_f32 v[92:93], v[96:97], v[92:93]
	s_mov_b32 s0, 0xf800000
	v_pk_add_f32 v[92:93], v[94:95], v[92:93]
	s_mov_b32 s3, 0x42fe0000
	v_add_f32_e32 v91, v92, v93
	s_waitcnt lgkmcnt(0)
	s_nop 1
	v_add_f32_dpp v91, v91, v91 quad_perm:[1,0,3,2] row_mask:0xf bank_mask:0xf
	v_readlane_b32 s40, v251, 5
	v_readlane_b32 s46, v251, 11
	v_readlane_b32 s47, v251, 12
	v_readlane_b32 s41, v251, 6
	s_nop 1
	v_add_f32_dpp v91, v91, v91 quad_perm:[2,3,0,1] row_mask:0xf bank_mask:0xf
	v_readlane_b32 s42, v251, 7
	v_readlane_b32 s43, v251, 8
	v_readlane_b32 s44, v251, 9
	v_readlane_b32 s45, v251, 10
	s_nop 1
	v_add_f32_dpp v91, v91, v91 row_half_mirror row_mask:0xf bank_mask:0xf
	s_nop 1
	v_add_f32_dpp v91, v91, v91 row_mirror row_mask:0xf bank_mask:0xf
	s_nop 1
	v_readlane_b32 s98, v91, 0
	v_readlane_b32 s99, v91, 16
	v_readlane_b32 s100, v91, 32
	v_readlane_b32 s101, v91, 48
	s_nop 1
	v_mov_b32_e32 v92, s99
	v_add_f32_e32 v92, s98, v92
	v_mov_b32_e32 v91, s101
	v_add_f32_e32 v91, s100, v91
	v_add_f32_e32 v91, v92, v91
	v_fmamk_f32 v91, v91, 0x3a800000, v241
	v_mul_f32_e32 v92, 0x4f800000, v91
	v_cmp_gt_f32_e32 vcc, s0, v91
	s_nop 1
	v_cndmask_b32_e32 v91, v91, v92, vcc
	v_sqrt_f32_e32 v94, v91
	v_pk_add_f32 v[92:93], v[28:29], 1.0 op_sel_hi:[1,0]
	v_add_u32_e32 v95, -1, v94
	v_add_u32_e32 v96, 1, v94
	v_fma_f32 v97, -v95, v94, v91
	v_fma_f32 v98, -v96, v94, v91
	v_cmp_ge_f32_e64 s[0:1], 0, v97
	s_nop 1
	v_cndmask_b32_e64 v94, v94, v95, s[0:1]
	v_cmp_lt_f32_e64 s[0:1], 0, v98
	s_nop 1
	v_cndmask_b32_e64 v94, v94, v96, s[0:1]
	v_mul_f32_e32 v95, 0x37800000, v94
	v_cndmask_b32_e32 v94, v94, v95, vcc
	v_cmp_class_f32_e32 vcc, v91, v188
	s_nop 1
	v_cndmask_b32_e32 v91, v94, v91, vcc
	v_div_scale_f32 v96, s[0:1], v91, v91, 1.0
	v_rcp_f32_e32 v97, v96
	v_div_scale_f32 v98, vcc, 1.0, v91, 1.0
	v_pk_add_f32 v[94:95], v[26:27], 1.0 op_sel_hi:[1,0]
	v_fma_f32 v99, -v96, v97, 1.0
	v_fmac_f32_e32 v97, v99, v97
	v_mul_f32_e32 v99, v98, v97
	v_fma_f32 v100, -v96, v99, v98
	v_fmac_f32_e32 v99, v100, v97
	v_fma_f32 v96, -v96, v99, v98
	v_div_fmas_f32 v96, v96, v97, v99
	v_div_fixup_f32 v96, v96, v91, 1.0
	v_pk_mul_f32 v[64:65], v[64:65], v[96:97] op_sel_hi:[1,0]
	v_pk_mul_f32 v[62:63], v[62:63], v[96:97] op_sel_hi:[1,0]
	v_pk_mul_f32 v[64:65], v[16:17], v[64:65]
	v_pk_mul_f32 v[62:63], v[14:15], v[62:63]
	v_pk_mul_f32 v[60:61], v[60:61], v[96:97] op_sel_hi:[1,0]
	v_pk_mul_f32 v[58:59], v[58:59], v[96:97] op_sel_hi:[1,0]
	v_pk_fma_f32 v[64:65], v[92:93], v[64:65], v[20:21]
	v_pk_fma_f32 v[62:63], v[94:95], v[62:63], v[18:19]
	v_pk_mul_f32 v[58:59], v[10:11], v[58:59]
	v_pk_mul_f32 v[60:61], v[12:13], v[60:61]
	v_pk_add_f32 v[92:93], v[24:25], 1.0 op_sel_hi:[1,0]
	v_pk_add_f32 v[94:95], v[22:23], 1.0 op_sel_hi:[1,0]
	v_pk_mul_f32 v[56:57], v[56:57], v[96:97] op_sel_hi:[1,0]
	v_pk_mul_f32 v[54:55], v[54:55], v[96:97] op_sel_hi:[1,0]
	v_pk_fma_f32 v[60:61], v[92:93], v[60:61], v[32:33]
	v_pk_fma_f32 v[58:59], v[94:95], v[58:59], v[30:31]
	v_pk_mul_f32 v[54:55], v[6:7], v[54:55]
	v_pk_mul_f32 v[56:57], v[8:9], v[56:57]
	v_pk_add_f32 v[92:93], v[40:41], 1.0 op_sel_hi:[1,0]
	v_pk_add_f32 v[94:95], v[38:39], 1.0 op_sel_hi:[1,0]
	v_pk_mul_f32 v[52:53], v[52:53], v[96:97] op_sel_hi:[1,0]
	v_pk_mul_f32 v[50:51], v[50:51], v[96:97] op_sel_hi:[1,0]
	v_pk_fma_f32 v[56:57], v[92:93], v[56:57], v[44:45]
	v_pk_fma_f32 v[54:55], v[94:95], v[54:55], v[42:43]
	v_pk_mul_f32 v[50:51], v[2:3], v[50:51]
	v_pk_mul_f32 v[52:53], v[4:5], v[52:53]
	v_pk_add_f32 v[92:93], v[36:37], 1.0 op_sel_hi:[1,0]
	v_pk_add_f32 v[94:95], v[34:35], 1.0 op_sel_hi:[1,0]
	v_pk_fma_f32 v[52:53], v[92:93], v[52:53], v[48:49]
	v_pk_fma_f32 v[92:93], v[94:95], v[50:51], v[46:47]
	v_max_f32_e64 v50, |v62|, |v63|
	v_max_f32_e64 v51, |v64|, |v65|
	v_max3_f32 v50, v50, 0, v51
	v_max_f32_e64 v51, |v58|, |v59|
	v_max_f32_e64 v91, |v60|, |v61|
	v_max3_f32 v50, v50, v51, v91
	v_max_f32_e64 v51, |v54|, |v55|
	v_max_f32_e64 v91, |v56|, |v57|
	v_max3_f32 v50, v50, v51, v91
	v_max_f32_e64 v51, |v92|, |v93|
	v_max_f32_e64 v91, |v52|, |v53|
	v_max3_f32 v50, v50, v51, v91
	s_waitcnt lgkmcnt(0)
	s_nop 1
	v_max_f32_dpp v50, v50, v50 quad_perm:[1,0,3,2] row_mask:0xf bank_mask:0xf
	s_nop 1
	v_max_f32_dpp v50, v50, v50 quad_perm:[2,3,0,1] row_mask:0xf bank_mask:0xf
	s_nop 1
	v_max_f32_dpp v50, v50, v50 row_half_mirror row_mask:0xf bank_mask:0xf
	s_nop 1
	v_max_f32_dpp v50, v50, v50 row_mirror row_mask:0xf bank_mask:0xf
	s_nop 1
	v_readlane_b32 s98, v50, 0
	v_readlane_b32 s99, v50, 16
	v_readlane_b32 s100, v50, 32
	v_readlane_b32 s101, v50, 48
	s_nop 1
	v_mov_b32_e32 v51, s99
	v_max_f32_e32 v51, s98, v51
	v_mov_b32_e32 v50, s101
	v_max_f32_e32 v50, s100, v50
	v_max_f32_e32 v50, v51, v50
	v_div_scale_f32 v51, s[0:1], v50, v50, s3
	v_rcp_f32_e32 v91, v51
	s_mov_b32 s0, 0x40c0c00
	s_mov_b32 s1, 0x8900000
	v_fma_f32 v94, -v51, v91, 1.0
	v_fmac_f32_e32 v91, v94, v91
	v_div_scale_f32 v94, vcc, s3, v50, s3
	v_mul_f32_e32 v95, v94, v91
	v_fma_f32 v96, -v51, v95, v94
	v_fmac_f32_e32 v95, v96, v91
	v_fma_f32 v51, -v51, v95, v94
	v_div_fmas_f32 v51, v51, v91, v95
	v_div_fixup_f32 v51, v51, v50, s3
	v_cmp_lt_f32_e32 vcc, 0, v50
	v_lshl_add_u64 v[94:95], s[46:47], 0, v[82:83]
	s_nop 0
	v_cndmask_b32_e32 v51, 0, v51, vcc
	v_mul_f32_e32 v63, v63, v51
	v_mul_f32_e32 v62, v62, v51
	v_rndne_f32_e32 v63, v63
	v_mul_f32_e32 v64, v64, v51
	v_mul_f32_e32 v65, v65, v51
	v_mul_f32_e32 v55, v55, v51
	v_rndne_f32_e32 v62, v62
	v_cvt_i32_f32_e32 v63, v63
	v_rndne_f32_e32 v64, v64
	v_rndne_f32_e32 v65, v65
	v_mul_f32_e32 v54, v54, v51
	v_rndne_f32_e32 v55, v55
	v_mul_f32_e32 v56, v56, v51
	v_mul_f32_e32 v57, v57, v51
	v_cvt_i32_f32_e32 v62, v62
	v_cvt_i32_f32_sdwa v64, v64 dst_sel:WORD_1 dst_unused:UNUSED_PAD src0_sel:DWORD
	v_cvt_i32_f32_e32 v65, v65
	v_rndne_f32_e32 v54, v54
	v_cvt_i32_f32_e32 v55, v55
	v_rndne_f32_e32 v56, v56
	v_rndne_f32_e32 v57, v57
	v_cvt_i32_f32_e32 v54, v54
	v_cvt_i32_f32_sdwa v56, v56 dst_sel:WORD_1 dst_unused:UNUSED_PAD src0_sel:DWORD
	v_cvt_i32_f32_e32 v57, v57
	v_lshlrev_b32_e32 v63, 8, v63
	v_and_b32_e32 v63, 0xff00, v63
	v_and_b32_e32 v64, 0xff0000, v64
	v_perm_b32 v62, v65, v62, s0
	v_lshlrev_b32_e32 v55, 8, v55
	v_or3_b32 v64, v62, v63, v64
	v_add_co_u32_e32 v62, vcc, s1, v94
	v_and_b32_e32 v55, 0xff00, v55
	v_and_b32_e32 v56, 0xff0000, v56
	v_perm_b32 v54, v57, v54, s0
	v_addc_co_u32_e32 v63, vcc, 0, v95, vcc
	v_mul_f32_e32 v59, v59, v51
	v_or3_b32 v54, v54, v55, v56
	v_mul_f32_e32 v55, v93, v51
	v_mul_f32_e32 v58, v58, v51
	v_rndne_f32_e32 v59, v59
	v_mul_f32_e32 v60, v60, v51
	v_mul_f32_e32 v61, v61, v51
	global_store_dword v[62:63], v54, off offset:512
	v_mul_f32_e32 v54, v92, v51
	v_rndne_f32_e32 v55, v55
	v_mul_f32_e32 v52, v52, v51
	v_mul_f32_e32 v51, v53, v51
	v_rndne_f32_e32 v58, v58
	v_cvt_i32_f32_e32 v59, v59
	v_rndne_f32_e32 v60, v60
	v_rndne_f32_e32 v61, v61
	v_rndne_f32_e32 v54, v54
	v_cvt_i32_f32_e32 v55, v55
	v_rndne_f32_e32 v52, v52
	v_rndne_f32_e32 v51, v51
	v_cvt_i32_f32_e32 v58, v58
	v_cvt_i32_f32_sdwa v60, v60 dst_sel:WORD_1 dst_unused:UNUSED_PAD src0_sel:DWORD
	v_cvt_i32_f32_e32 v61, v61
	v_cvt_i32_f32_e32 v54, v54
	v_cvt_i32_f32_sdwa v52, v52 dst_sel:WORD_1 dst_unused:UNUSED_PAD src0_sel:DWORD
	v_cvt_i32_f32_e32 v51, v51
	v_lshlrev_b32_e32 v59, 8, v59
	v_lshlrev_b32_e32 v53, 8, v55
	v_and_b32_e32 v59, 0xff00, v59
	v_and_b32_e32 v60, 0xff0000, v60
	v_perm_b32 v58, v61, v58, s0
	v_and_b32_e32 v53, 0xff00, v53
	v_and_b32_e32 v52, 0xff0000, v52
	v_perm_b32 v51, v51, v54, s0
	v_or3_b32 v58, v58, v59, v60
	v_or3_b32 v51, v51, v53, v52
	global_store_dword v[62:63], v64, off
	global_store_dword v[62:63], v58, off offset:256
	global_store_dword v[62:63], v51, off offset:768
	s_and_saveexec_b64 s[0:1], s[36:37]
	s_cbranch_execz .LBB0_383
	v_readlane_b32 s40, v251, 5
	v_readlane_b32 s46, v251, 11
	v_readlane_b32 s47, v251, 12
	v_mul_f32_e32 v52, 0x3c010204, v50
	v_readlane_b32 s41, v251, 6
	v_lshl_add_u64 v[50:51], s[46:47], 0, v[78:79]
	v_readlane_b32 s42, v251, 7
	v_readlane_b32 s43, v251, 8
	v_readlane_b32 s44, v251, 9
	v_readlane_b32 s45, v251, 10
	global_store_dword v[50:51], v52, off
	s_branch .LBB0_383

.LBB0_399:
	v_readlane_b32 s40, v251, 5
	v_readlane_b32 s46, v251, 11
	v_readlane_b32 s47, v251, 12
	s_mov_b32 s0, 0xf800000
	s_mov_b32 s3, 0x42fe0000
	v_lshl_add_u64 v[68:69], s[46:47], 0, v[88:89]
	v_add_co_u32_e32 v106, vcc, 0x500000, v68
	v_readlane_b32 s41, v251, 6
	s_nop 0
	v_addc_co_u32_e32 v107, vcc, 0, v69, vcc
	global_load_dwordx2 v[68:69], v[106:107], off
	global_load_dwordx2 v[70:71], v[106:107], off offset:512
	global_load_dwordx2 v[98:99], v[106:107], off offset:1024
	global_load_dwordx2 v[112:113], v[106:107], off offset:1536
	v_readlane_b32 s42, v251, 7
	v_readlane_b32 s43, v251, 8
	v_readlane_b32 s44, v251, 9
	v_readlane_b32 s45, v251, 10
	s_waitcnt vmcnt(3)
	v_lshlrev_b32_e32 v108, 16, v68
	v_and_b32_e32 v109, 0xffff0000, v68
	v_lshlrev_b32_e32 v96, 16, v69
	v_and_b32_e32 v97, 0xffff0000, v69
	v_lshl_add_u64 v[68:69], s[46:47], 0, v[84:85]
	s_waitcnt vmcnt(2)
	v_lshlrev_b32_e32 v94, 16, v70
	v_and_b32_e32 v95, 0xffff0000, v70
	v_lshlrev_b32_e32 v110, 16, v71
	v_and_b32_e32 v111, 0xffff0000, v71
	global_load_dwordx4 v[68:71], v[68:69], off
	s_waitcnt vmcnt(0)
	v_lshl_add_u64 v[68:69], s[46:47], 0, v[86:87]
	global_load_dwordx2 v[68:69], v[68:69], off
	v_lshlrev_b32_e32 v104, 16, v98
	v_and_b32_e32 v105, 0xffff0000, v98
	v_lshlrev_b32_e32 v102, 16, v99
	v_and_b32_e32 v103, 0xffff0000, v99
	v_lshlrev_b32_e32 v100, 16, v112
	v_and_b32_e32 v101, 0xffff0000, v112
	v_lshlrev_b32_e32 v98, 16, v113
	v_and_b32_e32 v99, 0xffff0000, v113
	v_mov_b32_e32 v128, v71
	s_waitcnt vmcnt(0)
	v_ashrrev_i32_e32 v113, 31, v68
	v_mov_b32_e32 v112, v68
	v_lshlrev_b64 v[112:113], 11, v[112:113]
	v_ashrrev_i32_e32 v115, 31, v69
	v_mov_b32_e32 v114, v69
	v_lshl_add_u64 v[112:113], v[82:83], 0, v[112:113]
	v_lshlrev_b64 v[68:69], 11, v[114:115]
	v_lshl_add_u64 v[114:115], v[82:83], 0, v[68:69]
	global_load_dwordx2 v[68:69], v[112:113], off
	global_load_dwordx2 v[122:123], v[114:115], off
	s_waitcnt vmcnt(1)
	v_lshlrev_b32_e32 v124, 16, v68
	s_waitcnt vmcnt(0)
	v_lshlrev_b32_e32 v126, 16, v122
	v_and_b32_e32 v127, 0xffff0000, v122
	v_lshlrev_b32_e32 v122, 16, v123
	v_and_b32_e32 v123, 0xffff0000, v123
	v_and_b32_e32 v125, 0xffff0000, v68
	v_lshlrev_b32_e32 v68, 16, v69
	v_and_b32_e32 v69, 0xffff0000, v69
	v_pk_mul_f32 v[122:123], v[128:129], v[122:123] op_sel_hi:[0,1]
	v_pk_mul_f32 v[126:127], v[128:129], v[126:127] op_sel_hi:[0,1]
	v_pk_fma_f32 v[124:125], v[70:71], v[124:125], v[126:127] op_sel_hi:[0,1,1]
	v_pk_fma_f32 v[68:69], v[70:71], v[68:69], v[122:123] op_sel_hi:[0,1,1]
	v_pk_fma_f32 v[96:97], v[64:65], v[68:69], v[96:97]
	v_pk_fma_f32 v[108:109], v[62:63], v[124:125], v[108:109]
	v_cvt_pk_bf16_f32 v69, v96, v97
	v_cvt_pk_bf16_f32 v68, v108, v109
	global_store_dwordx2 v[106:107], v[68:69], off
	global_load_dwordx2 v[68:69], v[112:113], off offset:512
	s_nop 0
	global_load_dwordx2 v[122:123], v[114:115], off offset:512
	s_waitcnt vmcnt(1)
	v_lshlrev_b32_e32 v124, 16, v68
	s_waitcnt vmcnt(0)
	v_lshlrev_b32_e32 v126, 16, v122
	v_and_b32_e32 v127, 0xffff0000, v122
	v_lshlrev_b32_e32 v122, 16, v123
	v_and_b32_e32 v123, 0xffff0000, v123
	v_and_b32_e32 v125, 0xffff0000, v68
	v_lshlrev_b32_e32 v68, 16, v69
	v_and_b32_e32 v69, 0xffff0000, v69
	v_pk_mul_f32 v[122:123], v[128:129], v[122:123] op_sel_hi:[0,1]
	v_pk_mul_f32 v[126:127], v[128:129], v[126:127] op_sel_hi:[0,1]
	v_pk_fma_f32 v[124:125], v[70:71], v[124:125], v[126:127] op_sel_hi:[0,1,1]
	v_pk_fma_f32 v[68:69], v[70:71], v[68:69], v[122:123] op_sel_hi:[0,1,1]
	v_pk_fma_f32 v[68:69], v[56:57], v[68:69], v[110:111]
	v_pk_fma_f32 v[94:95], v[54:55], v[124:125], v[94:95]
	v_cvt_pk_bf16_f32 v111, v68, v69
	v_cvt_pk_bf16_f32 v110, v94, v95
	global_store_dwordx2 v[106:107], v[110:111], off offset:512
	global_load_dwordx2 v[110:111], v[112:113], off offset:1024
	s_nop 0
	global_load_dwordx2 v[122:123], v[114:115], off offset:1024
	s_waitcnt vmcnt(1)
	v_lshlrev_b32_e32 v124, 16, v110
	s_waitcnt vmcnt(0)
	v_lshlrev_b32_e32 v126, 16, v122
	v_and_b32_e32 v127, 0xffff0000, v122
	v_lshlrev_b32_e32 v122, 16, v123
	v_and_b32_e32 v123, 0xffff0000, v123
	v_and_b32_e32 v125, 0xffff0000, v110
	v_lshlrev_b32_e32 v110, 16, v111
	v_and_b32_e32 v111, 0xffff0000, v111
	v_pk_mul_f32 v[122:123], v[128:129], v[122:123] op_sel_hi:[0,1]
	v_pk_mul_f32 v[126:127], v[128:129], v[126:127] op_sel_hi:[0,1]
	v_pk_fma_f32 v[124:125], v[70:71], v[124:125], v[126:127] op_sel_hi:[0,1,1]
	v_pk_fma_f32 v[110:111], v[70:71], v[110:111], v[122:123] op_sel_hi:[0,1,1]
	v_pk_fma_f32 v[102:103], v[52:53], v[110:111], v[102:103]
	v_pk_fma_f32 v[104:105], v[50:51], v[124:125], v[104:105]
	v_cvt_pk_bf16_f32 v111, v102, v103
	v_cvt_pk_bf16_f32 v110, v104, v105
	global_store_dwordx2 v[106:107], v[110:111], off offset:1024
	global_load_dwordx2 v[110:111], v[112:113], off offset:1536
	s_nop 0
	global_load_dwordx2 v[112:113], v[114:115], off offset:1536
	s_waitcnt vmcnt(1)
	v_lshlrev_b32_e32 v114, 16, v110
	s_waitcnt vmcnt(0)
	v_lshlrev_b32_e32 v122, 16, v112
	v_and_b32_e32 v123, 0xffff0000, v112
	v_lshlrev_b32_e32 v112, 16, v113
	v_and_b32_e32 v113, 0xffff0000, v113
	v_and_b32_e32 v115, 0xffff0000, v110
	v_lshlrev_b32_e32 v110, 16, v111
	v_and_b32_e32 v111, 0xffff0000, v111
	v_pk_mul_f32 v[112:113], v[128:129], v[112:113] op_sel_hi:[0,1]
	v_pk_mul_f32 v[122:123], v[128:129], v[122:123] op_sel_hi:[0,1]
	v_pk_fma_f32 v[114:115], v[70:71], v[114:115], v[122:123] op_sel_hi:[0,1,1]
	v_pk_fma_f32 v[70:71], v[70:71], v[110:111], v[112:113] op_sel_hi:[0,1,1]
	v_pk_fma_f32 v[98:99], v[60:61], v[70:71], v[98:99]
	v_pk_fma_f32 v[100:101], v[58:59], v[114:115], v[100:101]
	v_cvt_pk_bf16_f32 v71, v98, v99
	v_cvt_pk_bf16_f32 v70, v100, v101
	global_store_dwordx2 v[106:107], v[70:71], off offset:1536
	v_pk_mul_f32 v[70:71], v[96:97], v[96:97]
	v_pk_mul_f32 v[106:107], v[108:109], v[108:109]
	s_nop 0
	v_pk_mov_b32 v[110:111], v[106:107], v[70:71] op_sel:[1,0]
	v_mov_b32_e32 v107, v71
	v_pk_add_f32 v[70:71], v[110:111], v[106:107]
	v_pk_mul_f32 v[106:107], v[68:69], v[68:69]
	v_pk_mul_f32 v[110:111], v[94:95], v[94:95]
	v_pk_add_f32 v[70:71], v[70:71], v[70:71] op_sel:[0,1] op_sel_hi:[1,0]
	v_pk_mov_b32 v[112:113], v[110:111], v[106:107] op_sel:[1,0]
	v_mov_b32_e32 v111, v107
	v_pk_add_f32 v[106:107], v[112:113], v[110:111]
	v_mul_f32_e32 v110, v100, v100
	v_mul_f32_e32 v111, v101, v101
	v_pk_add_f32 v[106:107], v[106:107], v[106:107] op_sel:[0,1] op_sel_hi:[1,0]
	v_mov_b32_e32 v71, v110
	v_mov_b32_e32 v107, v111
	v_pk_add_f32 v[70:71], v[70:71], v[106:107]
	v_mul_f32_e32 v106, v105, v105
	v_mul_f32_e32 v110, v103, v103
	v_mul_f32_e32 v112, v98, v98
	v_mul_f32_e32 v113, v99, v99
	v_pk_fma_f32 v[106:107], v[104:105], v[104:105], v[106:107] op_sel_hi:[1,1,0]
	v_pk_fma_f32 v[110:111], v[102:103], v[102:103], v[110:111] op_sel_hi:[1,1,0]
	v_mov_b32_e32 v107, v112
	v_mov_b32_e32 v111, v113
	v_pk_add_f32 v[106:107], v[106:107], v[110:111]
	s_nop 0
	v_pk_add_f32 v[70:71], v[70:71], v[106:107]
	s_nop 0
	v_add_f32_e32 v70, v70, v71
	s_waitcnt lgkmcnt(0)
	s_nop 1
	v_add_f32_dpp v70, v70, v70 quad_perm:[1,0,3,2] row_mask:0xf bank_mask:0xf
	s_nop 1
	v_add_f32_dpp v70, v70, v70 quad_perm:[2,3,0,1] row_mask:0xf bank_mask:0xf
	s_nop 1
	v_add_f32_dpp v70, v70, v70 row_half_mirror row_mask:0xf bank_mask:0xf
	s_nop 1
	v_add_f32_dpp v70, v70, v70 row_mirror row_mask:0xf bank_mask:0xf
	s_nop 1
	v_readlane_b32 s98, v70, 0
	v_readlane_b32 s99, v70, 16
	v_readlane_b32 s100, v70, 32
	v_readlane_b32 s101, v70, 48
	s_nop 1
	v_mov_b32_e32 v71, s99
	v_add_f32_e32 v71, s98, v71
	v_mov_b32_e32 v70, s101
	v_add_f32_e32 v70, s100, v70
	v_add_f32_e32 v70, v71, v70
	v_fmamk_f32 v70, v70, 0x3a800000, v241
	v_cmp_gt_f32_e32 vcc, s0, v70
	v_mul_f32_e32 v71, 0x4f800000, v70
	s_nop 0
	v_cndmask_b32_e32 v70, v70, v71, vcc
	v_sqrt_f32_e32 v71, v70
	s_nop 0
	v_add_u32_e32 v106, -1, v71
	v_fma_f32 v107, -v106, v71, v70
	v_cmp_ge_f32_e64 s[0:1], 0, v107
	v_add_u32_e32 v107, 1, v71
	s_nop 0
	v_cndmask_b32_e64 v106, v71, v106, s[0:1]
	v_fma_f32 v71, -v107, v71, v70
	v_cmp_lt_f32_e64 s[0:1], 0, v71
	s_nop 1
	v_cndmask_b32_e64 v71, v106, v107, s[0:1]
	v_mul_f32_e32 v106, 0x37800000, v71
	v_cndmask_b32_e32 v71, v71, v106, vcc
	v_cmp_class_f32_e32 vcc, v70, v188
	s_nop 1
	v_cndmask_b32_e32 v70, v71, v70, vcc
	v_div_scale_f32 v71, s[0:1], v70, v70, 1.0
	v_rcp_f32_e32 v106, v71
	s_nop 0
	v_fma_f32 v107, -v71, v106, 1.0
	v_fmac_f32_e32 v106, v107, v106
	v_div_scale_f32 v107, vcc, 1.0, v70, 1.0
	v_mul_f32_e32 v110, v107, v106
	v_fma_f32 v111, -v71, v110, v107
	v_fmac_f32_e32 v110, v111, v106
	v_fma_f32 v71, -v71, v110, v107
	v_div_fmas_f32 v71, v71, v106, v110
	v_div_fixup_f32 v110, v71, v70, 1.0
	v_pk_mul_f32 v[70:71], v[96:97], v[110:111] op_sel_hi:[1,0]
	v_pk_add_f32 v[106:107], v[20:21], 1.0 op_sel_hi:[1,0]
	v_pk_mul_f32 v[70:71], v[16:17], v[70:71]
	v_pk_mul_f32 v[96:97], v[108:109], v[110:111] op_sel_hi:[1,0]
	v_pk_fma_f32 v[106:107], v[106:107], v[70:71], v[40:41]
	v_pk_mul_f32 v[68:69], v[68:69], v[110:111] op_sel_hi:[1,0]
	v_pk_mul_f32 v[70:71], v[94:95], v[110:111] op_sel_hi:[1,0]
	v_pk_mul_f32 v[96:97], v[14:15], v[96:97]
	v_pk_add_f32 v[108:109], v[18:19], 1.0 op_sel_hi:[1,0]
	v_pk_mul_f32 v[94:95], v[10:11], v[70:71]
	v_pk_mul_f32 v[68:69], v[12:13], v[68:69]
	v_pk_add_f32 v[70:71], v[24:25], 1.0 op_sel_hi:[1,0]
	v_pk_fma_f32 v[108:109], v[108:109], v[96:97], v[38:39]
	v_pk_add_f32 v[96:97], v[22:23], 1.0 op_sel_hi:[1,0]
	v_pk_fma_f32 v[70:71], v[70:71], v[68:69], v[36:37]
	v_pk_mul_f32 v[68:69], v[102:103], v[110:111] op_sel_hi:[1,0]
	v_pk_fma_f32 v[96:97], v[96:97], v[94:95], v[34:35]
	v_pk_mul_f32 v[94:95], v[104:105], v[110:111] op_sel_hi:[1,0]
	v_pk_mul_f32 v[68:69], v[8:9], v[68:69]
	v_pk_add_f32 v[102:103], v[32:33], 1.0 op_sel_hi:[1,0]
	v_pk_mul_f32 v[98:99], v[98:99], v[110:111] op_sel_hi:[1,0]
	v_pk_mul_f32 v[94:95], v[6:7], v[94:95]
	v_pk_add_f32 v[104:105], v[30:31], 1.0 op_sel_hi:[1,0]
	v_pk_fma_f32 v[68:69], v[102:103], v[68:69], v[44:45]
	v_pk_mul_f32 v[100:101], v[100:101], v[110:111] op_sel_hi:[1,0]
	v_pk_mul_f32 v[98:99], v[4:5], v[98:99]
	v_pk_add_f32 v[102:103], v[28:29], 1.0 op_sel_hi:[1,0]
	v_pk_fma_f32 v[94:95], v[104:105], v[94:95], v[42:43]
	v_pk_mul_f32 v[100:101], v[2:3], v[100:101]
	v_pk_add_f32 v[104:105], v[26:27], 1.0 op_sel_hi:[1,0]
	v_pk_fma_f32 v[98:99], v[102:103], v[98:99], v[48:49]
	v_max_f32_e64 v102, |v108|, |v109|
	v_max_f32_e64 v103, |v106|, |v107|
	v_pk_fma_f32 v[100:101], v[104:105], v[100:101], v[46:47]
	v_max3_f32 v102, v102, 0, v103
	v_max_f32_e64 v103, |v96|, |v97|
	v_max_f32_e64 v104, |v70|, |v71|
	v_max3_f32 v102, v102, v103, v104
	v_max_f32_e64 v103, |v94|, |v95|
	v_max_f32_e64 v104, |v68|, |v69|
	v_max3_f32 v102, v102, v103, v104
	v_max_f32_e64 v103, |v100|, |v101|
	v_max_f32_e64 v104, |v98|, |v99|
	v_max3_f32 v102, v102, v103, v104
	ds_bpermute_b32 v103, v1, v102
	s_waitcnt lgkmcnt(0)
	v_max_f32_e32 v103, v103, v103
	v_max_f32_e32 v102, v102, v103
	ds_bpermute_b32 v103, v116, v102
	s_waitcnt lgkmcnt(0)
	v_max_f32_e32 v103, v103, v103
	v_max_f32_e32 v102, v102, v103
	ds_bpermute_b32 v103, v117, v102
	s_waitcnt lgkmcnt(0)
	v_max_f32_e32 v103, v103, v103
	v_max_f32_e32 v102, v102, v103
	ds_bpermute_b32 v103, v118, v102
	s_waitcnt lgkmcnt(0)
	v_max_f32_e32 v103, v103, v103
	v_max_f32_e32 v102, v102, v103
	ds_bpermute_b32 v103, v119, v102
	s_waitcnt lgkmcnt(0)
	v_max_f32_e32 v103, v103, v103
	v_max_f32_e32 v102, v102, v103
	ds_bpermute_b32 v103, v120, v102
	s_waitcnt lgkmcnt(0)
	v_max_f32_e32 v103, v103, v103
	v_max_f32_e32 v104, v102, v103
	v_div_scale_f32 v102, s[10:11], v104, v104, s3
	v_rcp_f32_e32 v103, v102
	v_cmp_lt_f32_e64 s[0:1], 0, v104
	v_fma_f32 v105, -v102, v103, 1.0
	v_fmac_f32_e32 v103, v105, v103
	v_div_scale_f32 v105, vcc, s3, v104, s3
	v_mul_f32_e32 v110, v105, v103
	v_fma_f32 v111, -v102, v110, v105
	v_fmac_f32_e32 v110, v111, v103
	v_fma_f32 v102, -v102, v110, v105
	v_div_fmas_f32 v102, v102, v103, v110
	v_div_fixup_f32 v102, v102, v104, s3
	v_cndmask_b32_e64 v105, 0, v102, s[0:1]
	v_mul_f32_e32 v97, v97, v105
	v_mul_f32_e32 v96, v96, v105
	v_rndne_f32_e32 v97, v97
	v_mul_f32_e32 v70, v70, v105
	v_mul_f32_e32 v71, v71, v105
	v_rndne_f32_e32 v96, v96
	v_cvt_i32_f32_e32 v97, v97
	v_rndne_f32_e32 v70, v70
	v_rndne_f32_e32 v71, v71
	v_cvt_i32_f32_e32 v96, v96
	v_cvt_i32_f32_sdwa v70, v70 dst_sel:WORD_1 dst_unused:UNUSED_PAD src0_sel:DWORD
	v_cvt_i32_f32_e32 v71, v71
	v_lshl_add_u64 v[102:103], s[46:47], 0, v[90:91]
	s_mov_b32 s0, 0x40c0c00
	s_mov_b32 s1, 0x8900000
	v_lshlrev_b32_e32 v97, 8, v97
	v_add_co_u32_e32 v102, vcc, s1, v102
	v_and_b32_e32 v97, 0xff00, v97
	v_and_b32_e32 v70, 0xff0000, v70
	v_perm_b32 v71, v71, v96, s0
	v_addc_co_u32_e32 v103, vcc, 0, v103, vcc
	v_or3_b32 v70, v71, v97, v70
	v_mul_f32_e32 v71, v95, v105
	global_store_dword v[102:103], v70, off offset:256
	v_mul_f32_e32 v70, v94, v105
	v_rndne_f32_e32 v71, v71
	v_mul_f32_e32 v68, v68, v105
	v_mul_f32_e32 v69, v69, v105
	v_rndne_f32_e32 v70, v70
	v_cvt_i32_f32_e32 v71, v71
	v_rndne_f32_e32 v68, v68
	v_rndne_f32_e32 v69, v69
	v_cvt_i32_f32_e32 v70, v70
	v_cvt_i32_f32_sdwa v68, v68 dst_sel:WORD_1 dst_unused:UNUSED_PAD src0_sel:DWORD
	v_cvt_i32_f32_e32 v69, v69
	v_lshlrev_b32_e32 v71, 8, v71
	v_and_b32_e32 v71, 0xff00, v71
	v_and_b32_e32 v68, 0xff0000, v68
	v_perm_b32 v69, v69, v70, s0
	v_mul_f32_e32 v109, v109, v105
	v_or3_b32 v68, v69, v71, v68
	v_mul_f32_e32 v69, v101, v105
	v_mul_f32_e32 v108, v108, v105
	v_rndne_f32_e32 v109, v109
	v_mul_f32_e32 v106, v106, v105
	v_mul_f32_e32 v107, v107, v105
	global_store_dword v[102:103], v68, off offset:512
	v_mul_f32_e32 v68, v100, v105
	v_rndne_f32_e32 v69, v69
	v_mul_f32_e32 v70, v98, v105
	v_mul_f32_e32 v71, v99, v105
	v_rndne_f32_e32 v108, v108
	v_cvt_i32_f32_e32 v109, v109
	v_rndne_f32_e32 v106, v106
	v_rndne_f32_e32 v107, v107
	v_rndne_f32_e32 v68, v68
	v_cvt_i32_f32_e32 v69, v69
	v_rndne_f32_e32 v70, v70
	v_rndne_f32_e32 v71, v71
	v_cvt_i32_f32_e32 v108, v108
	v_cvt_i32_f32_sdwa v106, v106 dst_sel:WORD_1 dst_unused:UNUSED_PAD src0_sel:DWORD
	v_cvt_i32_f32_e32 v107, v107
	v_cvt_i32_f32_e32 v68, v68
	v_cvt_i32_f32_sdwa v70, v70 dst_sel:WORD_1 dst_unused:UNUSED_PAD src0_sel:DWORD
	v_cvt_i32_f32_e32 v71, v71
	v_lshlrev_b32_e32 v109, 8, v109
	v_lshlrev_b32_e32 v69, 8, v69
	v_and_b32_e32 v109, 0xff00, v109
	v_and_b32_e32 v106, 0xff0000, v106
	v_perm_b32 v107, v107, v108, s0
	v_and_b32_e32 v69, 0xff00, v69
	v_and_b32_e32 v70, 0xff0000, v70
	v_perm_b32 v68, v71, v68, s0
	v_or3_b32 v106, v107, v109, v106
	v_or3_b32 v68, v68, v69, v70
	global_store_dword v[102:103], v106, off
	global_store_dword v[102:103], v68, off offset:768
	s_and_saveexec_b64 s[0:1], s[36:37]
	s_cbranch_execz .LBB0_396
	v_readlane_b32 s40, v251, 5
	v_readlane_b32 s46, v251, 11
	v_readlane_b32 s47, v251, 12
	v_mul_f32_e32 v70, 0x3c010204, v104
	v_readlane_b32 s41, v251, 6
	v_lshl_add_u64 v[68:69], s[46:47], 0, v[92:93]
	v_readlane_b32 s42, v251, 7
	v_readlane_b32 s43, v251, 8
	v_readlane_b32 s44, v251, 9
	v_readlane_b32 s45, v251, 10
	global_store_dword v[68:69], v70, off
	s_branch .LBB0_396

.LBB0_1084:
	v_readlane_b32 s40, v251, 5
	v_readlane_b32 s46, v251, 11
	v_readlane_b32 s47, v251, 12
	s_mov_b64 s[0:1], 0x40590000
	s_mov_b32 s8, 0x42fe0000
	v_lshl_add_u64 v[28:29], s[46:47], 0, v[16:17]
	v_lshl_add_u64 v[2:3], v[28:29], 0, s[0:1]
	s_mov_b64 s[0:1], 0x40590800
	v_add_co_u32_e32 v6, vcc, 0x40590000, v28
	v_lshl_add_u64 v[8:9], v[28:29], 0, s[0:1]
	s_mov_b64 s[0:1], 0x40591000
	v_addc_co_u32_e32 v7, vcc, 0, v29, vcc
	v_lshl_add_u64 v[40:41], v[28:29], 0, s[0:1]
	s_mov_b32 s0, 0x40591000
	v_add_co_u32_e32 v28, vcc, s0, v28
	global_load_dwordx4 v[32:35], v[6:7], off
	s_nop 0
	global_load_dwordx4 v[2:5], v[2:3], off offset:16
	v_addc_co_u32_e32 v29, vcc, 0, v29, vcc
	global_load_dwordx4 v[36:39], v[6:7], off offset:2048
	s_nop 0
	global_load_dwordx4 v[6:9], v[8:9], off offset:16
	s_nop 0
	global_load_dwordx4 v[28:31], v[28:29], off
	s_nop 0
	global_load_dwordx4 v[40:43], v[40:41], off offset:16
	v_readlane_b32 s41, v251, 6
	v_readlane_b32 s42, v251, 7
	v_readlane_b32 s43, v251, 8
	v_readlane_b32 s44, v251, 9
	v_readlane_b32 s45, v251, 10
	s_waitcnt vmcnt(1)
	v_lshlrev_b32_e32 v45, 16, v30
	v_and_b32_e32 v46, 0xffff0000, v30
	v_lshlrev_b32_e32 v47, 16, v31
	v_and_b32_e32 v48, 0xffff0000, v31
	v_lshlrev_b32_e32 v30, 16, v32
	v_lshlrev_b32_e32 v31, 16, v36
	v_lshlrev_b32_e32 v27, 16, v28
	v_add_f32_e32 v30, v31, v30
	v_add_f32_e32 v49, v30, v27
	v_and_b32_e32 v27, 0xffff0000, v36
	v_and_b32_e32 v30, 0xffff0000, v32
	v_and_b32_e32 v28, 0xffff0000, v28
	v_add_f32_e32 v27, v27, v30
	v_add_f32_e32 v36, v27, v28
	v_lshlrev_b32_e32 v27, 16, v33
	v_lshlrev_b32_e32 v28, 16, v37
	v_lshlrev_b32_e32 v44, 16, v29
	v_add_f32_e32 v27, v28, v27
	v_add_f32_e32 v32, v27, v44
	v_and_b32_e32 v27, 0xffff0000, v37
	v_and_b32_e32 v28, 0xffff0000, v33
	v_and_b32_e32 v29, 0xffff0000, v29
	v_add_f32_e32 v27, v27, v28
	v_add_f32_e32 v31, v27, v29
	v_lshlrev_b32_e32 v27, 16, v34
	v_lshlrev_b32_e32 v28, 16, v38
	v_add_f32_e32 v27, v28, v27
	v_add_f32_e32 v30, v27, v45
	v_and_b32_e32 v27, 0xffff0000, v38
	v_and_b32_e32 v28, 0xffff0000, v34
	v_add_f32_e32 v27, v27, v28
	v_add_f32_e32 v29, v27, v46
	v_lshlrev_b32_e32 v27, 16, v35
	v_lshlrev_b32_e32 v28, 16, v39
	v_add_f32_e32 v27, v28, v27
	v_add_f32_e32 v28, v27, v47
	v_and_b32_e32 v27, 0xffff0000, v39
	v_and_b32_e32 v33, 0xffff0000, v35
	v_add_f32_e32 v27, v27, v33
	s_waitcnt vmcnt(0)
	v_lshlrev_b32_e32 v33, 16, v40
	v_and_b32_e32 v34, 0xffff0000, v40
	v_lshlrev_b32_e32 v35, 16, v41
	v_and_b32_e32 v37, 0xffff0000, v41
	v_lshlrev_b32_e32 v38, 16, v42
	v_and_b32_e32 v39, 0xffff0000, v42
	v_lshlrev_b32_e32 v40, 16, v43
	v_and_b32_e32 v41, 0xffff0000, v43
	v_lshlrev_b32_e32 v42, 16, v2
	v_lshlrev_b32_e32 v43, 16, v6
	v_and_b32_e32 v6, 0xffff0000, v6
	v_and_b32_e32 v2, 0xffff0000, v2
	v_add_f32_e32 v2, v6, v2
	v_add_f32_e32 v6, v2, v34
	v_lshlrev_b32_e32 v2, 16, v3
	v_lshlrev_b32_e32 v34, 16, v7
	v_add_f32_e32 v2, v34, v2
	v_add_f32_e32 v34, v2, v35
	v_and_b32_e32 v2, 0xffff0000, v7
	v_and_b32_e32 v3, 0xffff0000, v3
	v_add_f32_e32 v2, v2, v3
	v_add_f32_e32 v3, v2, v37
	v_lshlrev_b32_e32 v2, 16, v4
	v_lshlrev_b32_e32 v7, 16, v8
	v_add_f32_e32 v2, v7, v2
	v_add_f32_e32 v7, v2, v38
	v_and_b32_e32 v2, 0xffff0000, v8
	v_and_b32_e32 v4, 0xffff0000, v4
	v_add_f32_e32 v2, v2, v4
	v_add_f32_e32 v8, v2, v39
	v_lshlrev_b32_e32 v2, 16, v5
	v_lshlrev_b32_e32 v4, 16, v9
	v_add_f32_e32 v2, v4, v2
	v_add_f32_e32 v35, v2, v40
	v_and_b32_e32 v2, 0xffff0000, v9
	v_and_b32_e32 v4, 0xffff0000, v5
	v_add_f32_e32 v2, v2, v4
	v_add_f32_e32 v9, v2, v41
	v_max3_f32 v2, |v49|, 0, |v36|
	v_max3_f32 v2, v2, |v32|, |v31|
	v_add_f32_e32 v27, v27, v48
	v_add_f32_e32 v42, v43, v42
	v_max3_f32 v2, v2, |v30|, |v29|
	v_add_f32_e32 v33, v42, v33
	v_max3_f32 v2, v2, |v28|, |v27|
	v_max3_f32 v2, v2, |v33|, |v6|
	v_max3_f32 v2, v2, |v34|, |v3|
	v_max3_f32 v2, v2, |v7|, |v8|
	v_max3_f32 v2, v2, |v35|, |v9|
	s_waitcnt lgkmcnt(0)
	s_nop 1
	v_max_f32_dpp v2, v2, v2 quad_perm:[1,0,3,2] row_mask:0xf bank_mask:0xf
	s_nop 1
	v_max_f32_dpp v2, v2, v2 quad_perm:[2,3,0,1] row_mask:0xf bank_mask:0xf
	s_nop 1
	v_max_f32_dpp v2, v2, v2 row_half_mirror row_mask:0xf bank_mask:0xf
	s_nop 1
	v_max_f32_dpp v2, v2, v2 row_mirror row_mask:0xf bank_mask:0xf
	s_nop 1
	v_readlane_b32 s98, v2, 0
	v_readlane_b32 s99, v2, 16
	v_readlane_b32 s100, v2, 32
	v_readlane_b32 s101, v2, 48
	s_nop 1
	v_mov_b32_e32 v4, s99
	v_max_f32_e32 v4, s98, v4
	v_mov_b32_e32 v2, s101
	v_max_f32_e32 v2, s100, v2
	v_max_f32_e32 v2, v4, v2
	v_div_scale_f32 v4, s[4:5], v2, v2, s8
	v_rcp_f32_e32 v5, v4
	v_cmp_lt_f32_e64 s[0:1], 0, v2
	v_fma_f32 v37, -v4, v5, 1.0
	v_fmac_f32_e32 v5, v37, v5
	v_div_scale_f32 v37, vcc, s8, v2, s8
	v_mul_f32_e32 v38, v37, v5
	v_fma_f32 v39, -v4, v38, v37
	v_fmac_f32_e32 v38, v39, v5
	v_fma_f32 v4, -v4, v38, v37
	v_div_fmas_f32 v4, v4, v5, v38
	v_div_fixup_f32 v4, v4, v2, s8
	v_cndmask_b32_e64 v37, 0, v4, s[0:1]
	v_mul_f32_e32 v5, v36, v37
	v_mul_f32_e32 v4, v49, v37
	v_rndne_f32_e32 v5, v5
	v_mul_f32_e32 v32, v32, v37
	v_mul_f32_e32 v31, v31, v37
	v_rndne_f32_e32 v4, v4
	v_cvt_i32_f32_e32 v5, v5
	v_rndne_f32_e32 v32, v32
	v_rndne_f32_e32 v31, v31
	v_cvt_i32_f32_e32 v4, v4
	v_cvt_i32_f32_sdwa v32, v32 dst_sel:WORD_1 dst_unused:UNUSED_PAD src0_sel:DWORD
	v_cvt_i32_f32_e32 v31, v31
	v_lshlrev_b32_e32 v5, 8, v5
	s_mov_b32 s0, 0x40c0c00
	v_and_b32_e32 v5, 0xff00, v5
	v_and_b32_e32 v32, 0xff0000, v32
	v_perm_b32 v4, v31, v4, s0
	v_mul_f32_e32 v29, v29, v37
	v_or3_b32 v4, v4, v5, v32
	v_mul_f32_e32 v5, v30, v37
	v_rndne_f32_e32 v29, v29
	v_mul_f32_e32 v28, v28, v37
	v_mul_f32_e32 v27, v27, v37
	v_rndne_f32_e32 v5, v5
	v_cvt_i32_f32_e32 v29, v29
	v_rndne_f32_e32 v28, v28
	v_rndne_f32_e32 v27, v27
	v_cvt_i32_f32_e32 v5, v5
	v_cvt_i32_f32_sdwa v28, v28 dst_sel:WORD_1 dst_unused:UNUSED_PAD src0_sel:DWORD
	v_cvt_i32_f32_e32 v27, v27
	v_lshlrev_b32_e32 v29, 8, v29
	v_and_b32_e32 v29, 0xff00, v29
	v_and_b32_e32 v28, 0xff0000, v28
	v_perm_b32 v5, v27, v5, s0
	v_mul_f32_e32 v6, v6, v37
	v_or3_b32 v5, v5, v29, v28
	v_mul_f32_e32 v27, v33, v37
	v_rndne_f32_e32 v6, v6
	v_mul_f32_e32 v28, v34, v37
	v_mul_f32_e32 v3, v3, v37
	v_rndne_f32_e32 v27, v27
	v_cvt_i32_f32_e32 v6, v6
	v_rndne_f32_e32 v28, v28
	v_rndne_f32_e32 v3, v3
	v_cvt_i32_f32_e32 v27, v27
	v_cvt_i32_f32_sdwa v28, v28 dst_sel:WORD_1 dst_unused:UNUSED_PAD src0_sel:DWORD
	v_cvt_i32_f32_e32 v3, v3
	v_lshlrev_b32_e32 v6, 8, v6
	v_and_b32_e32 v6, 0xff00, v6
	v_and_b32_e32 v28, 0xff0000, v28
	v_perm_b32 v3, v3, v27, s0
	v_or3_b32 v6, v3, v6, v28
	v_mul_f32_e32 v3, v7, v37
	v_mul_f32_e32 v7, v8, v37
	v_rndne_f32_e32 v7, v7
	v_mul_f32_e32 v8, v35, v37
	v_mul_f32_e32 v9, v9, v37
	v_rndne_f32_e32 v3, v3
	v_cvt_i32_f32_e32 v7, v7
	v_rndne_f32_e32 v8, v8
	v_rndne_f32_e32 v9, v9
	v_cvt_i32_f32_e32 v3, v3
	v_cvt_i32_f32_sdwa v8, v8 dst_sel:WORD_1 dst_unused:UNUSED_PAD src0_sel:DWORD
	v_cvt_i32_f32_e32 v9, v9
	v_lshlrev_b32_e32 v7, 8, v7
	v_and_b32_e32 v7, 0xff00, v7
	v_and_b32_e32 v8, 0xff0000, v8
	v_perm_b32 v3, v9, v3, s0
	v_or3_b32 v7, v3, v7, v8
	v_lshl_add_u64 v[8:9], s[46:47], 0, v[12:13]
	global_store_dwordx4 v[8:9], v[4:7], off
	s_and_saveexec_b64 s[0:1], s[36:37]
	s_cbranch_execz .LBB0_1083
	v_readlane_b32 s40, v251, 5
	v_readlane_b32 s46, v251, 11
	v_readlane_b32 s47, v251, 12
	v_mul_f32_e32 v4, 0x3c010204, v2
	v_readlane_b32 s41, v251, 6
	v_lshl_add_u64 v[2:3], s[46:47], 0, v[20:21]
	v_readlane_b32 s42, v251, 7
	v_readlane_b32 s43, v251, 8
	v_readlane_b32 s44, v251, 9
	v_readlane_b32 s45, v251, 10
	global_store_dword v[2:3], v4, off
	s_branch .LBB0_1083

.LBB0_1217:
	global_load_dwordx2 v[184:185], v[198:199], off offset:-1024
	global_load_dwordx2 v[186:187], v[198:199], off offset:-512
	global_load_dwordx2 v[206:207], v[198:199], off
	global_load_dwordx2 v[208:209], v[198:199], off offset:512
	s_mov_b32 s0, 0xf800000
	s_mov_b32 s10, 0x42fe0000
	s_waitcnt vmcnt(2) lgkmcnt(3)
	v_and_b32_e32 v215, 0xffff0000, v187
	v_and_b32_e32 v214, 0xffff0000, v186
	s_waitcnt vmcnt(0) lgkmcnt(0)
	v_lshlrev_b32_e32 v221, 16, v208
	v_and_b32_e32 v219, 0xffff0000, v208
	v_lshlrev_b32_e32 v222, 16, v209
	v_and_b32_e32 v223, 0xffff0000, v209
	v_lshlrev_b32_e32 v208, 16, v184
	v_and_b32_e32 v209, 0xffff0000, v184
	v_lshlrev_b32_e32 v184, 16, v185
	v_and_b32_e32 v185, 0xffff0000, v185
	v_mul_f32_e32 v210, v185, v185
	v_pk_fma_f32 v[228:229], v[184:185], v[184:185], v[210:211] op_sel_hi:[1,1,0]
	v_lshlrev_b32_e32 v210, 16, v206
	v_and_b32_e32 v211, 0xffff0000, v206
	v_mul_f32_e32 v206, v209, v209
	v_lshlrev_b32_e32 v213, 16, v187
	v_lshlrev_b32_e32 v212, 16, v186
	v_pk_mul_f32 v[186:187], v[214:215], v[214:215]
	v_lshlrev_b32_e32 v216, 16, v207
	v_and_b32_e32 v217, 0xffff0000, v207
	v_pk_fma_f32 v[206:207], v[208:209], v[208:209], v[206:207] op_sel_hi:[1,1,0]
	v_pk_fma_f32 v[186:187], v[212:213], v[212:213], v[186:187]
	v_mov_b32_e32 v220, v206
	v_mov_b32_e32 v230, v228
	v_mov_b32_e32 v231, v221
	v_mul_f32_e32 v218, v219, v219
	v_pk_add_f32 v[206:207], v[206:207], v[228:229]
	v_pk_mul_f32 v[228:229], v[220:221], v[230:231]
	v_pk_add_f32 v[186:187], v[186:187], v[186:187] op_sel:[0,1] op_sel_hi:[1,0]
	v_mov_b32_e32 v207, v229
	v_mov_b32_e32 v187, v218
	v_pk_add_f32 v[186:187], v[206:207], v[186:187]
	v_mul_f32_e32 v206, v211, v211
	v_mul_f32_e32 v218, v217, v217
	v_mul_f32_e32 v227, v222, v222
	v_mul_f32_e32 v232, v223, v223
	v_pk_fma_f32 v[206:207], v[210:211], v[210:211], v[206:207] op_sel_hi:[1,1,0]
	v_pk_fma_f32 v[228:229], v[216:217], v[216:217], v[218:219] op_sel_hi:[1,1,0]
	v_mov_b32_e32 v207, v227
	v_mov_b32_e32 v229, v232
	v_pk_add_f32 v[206:207], v[206:207], v[228:229]
	s_nop 0
	v_pk_add_f32 v[186:187], v[186:187], v[206:207]
	s_nop 0
	v_add_f32_e32 v186, v186, v187
	s_waitcnt lgkmcnt(0)
	s_nop 1
	v_add_f32_dpp v186, v186, v186 quad_perm:[1,0,3,2] row_mask:0xf bank_mask:0xf
	s_nop 1
	v_add_f32_dpp v186, v186, v186 quad_perm:[2,3,0,1] row_mask:0xf bank_mask:0xf
	s_nop 1
	v_add_f32_dpp v186, v186, v186 row_half_mirror row_mask:0xf bank_mask:0xf
	s_nop 1
	v_add_f32_dpp v186, v186, v186 row_mirror row_mask:0xf bank_mask:0xf
	s_nop 1
	v_readlane_b32 s98, v186, 0
	v_readlane_b32 s99, v186, 16
	v_readlane_b32 s100, v186, 32
	v_readlane_b32 s101, v186, 48
	s_nop 1
	v_mov_b32_e32 v187, s99
	v_add_f32_e32 v187, s98, v187
	v_mov_b32_e32 v186, s101
	v_add_f32_e32 v186, s100, v186
	v_add_f32_e32 v186, v187, v186
	v_fmamk_f32 v186, v186, 0x3a800000, v241
	v_cmp_gt_f32_e32 vcc, s0, v186
	v_mul_f32_e32 v187, 0x4f800000, v186
	s_nop 0
	v_cndmask_b32_e32 v186, v186, v187, vcc
	v_sqrt_f32_e32 v187, v186
	s_nop 0
	v_add_u32_e32 v206, -1, v187
	v_fma_f32 v207, -v206, v187, v186
	v_cmp_ge_f32_e64 s[0:1], 0, v207
	v_add_u32_e32 v207, 1, v187
	s_nop 0
	v_cndmask_b32_e64 v206, v187, v206, s[0:1]
	v_fma_f32 v187, -v207, v187, v186
	v_cmp_lt_f32_e64 s[0:1], 0, v187
	s_nop 1
	v_cndmask_b32_e64 v187, v206, v207, s[0:1]
	v_mul_f32_e32 v206, 0x37800000, v187
	v_cndmask_b32_e32 v187, v187, v206, vcc
	v_cmp_class_f32_e32 vcc, v186, v188
	s_nop 1
	v_cndmask_b32_e32 v186, v187, v186, vcc
	v_div_scale_f32 v187, s[0:1], v186, v186, 1.0
	v_rcp_f32_e32 v206, v187
	s_nop 0
	v_fma_f32 v207, -v187, v206, 1.0
	v_fmac_f32_e32 v206, v207, v206
	v_div_scale_f32 v207, vcc, 1.0, v186, 1.0
	v_mul_f32_e32 v218, v207, v206
	v_fma_f32 v220, -v187, v218, v207
	v_fmac_f32_e32 v218, v220, v206
	v_fma_f32 v187, -v187, v218, v207
	v_div_fmas_f32 v187, v187, v206, v218
	v_div_fixup_f32 v220, v187, v186, 1.0
	v_pk_mul_f32 v[184:185], v[220:221], v[184:185] op_sel_hi:[0,1]
	v_pk_mul_f32 v[184:185], v[4:5], v[184:185]
	v_pk_add_f32 v[206:207], v[150:151], 1.0 op_sel_hi:[1,0]
	v_pk_mul_f32 v[186:187], v[220:221], v[208:209] op_sel_hi:[0,1]
	v_pk_fma_f32 v[206:207], v[206:207], v[184:185], v[162:163]
	v_mov_b32_e32 v184, v213
	v_mov_b32_e32 v185, v215
	v_pk_mul_f32 v[186:187], v[2:3], v[186:187]
	v_pk_add_f32 v[208:209], v[148:149], 1.0 op_sel_hi:[1,0]
	v_pk_mul_f32 v[184:185], v[220:221], v[184:185] op_sel_hi:[0,1]
	v_mov_b32_e32 v213, v214
	v_pk_fma_f32 v[208:209], v[208:209], v[186:187], v[160:161]
	v_pk_mul_f32 v[186:187], v[220:221], v[212:213] op_sel_hi:[0,1]
	v_pk_mul_f32 v[184:185], v[8:9], v[184:185]
	v_pk_add_f32 v[212:213], v[154:155], 1.0 op_sel_hi:[1,0]
	v_pk_mul_f32 v[186:187], v[6:7], v[186:187]
	v_pk_add_f32 v[214:215], v[152:153], 1.0 op_sel_hi:[1,0]
	v_pk_fma_f32 v[212:213], v[212:213], v[184:185], v[158:159]
	v_pk_mul_f32 v[184:185], v[220:221], v[216:217] op_sel_hi:[0,1]
	v_pk_fma_f32 v[214:215], v[214:215], v[186:187], v[156:157]
	v_pk_mul_f32 v[186:187], v[220:221], v[210:211] op_sel_hi:[0,1]
	v_pk_mul_f32 v[184:185], v[12:13], v[184:185]
	v_pk_add_f32 v[210:211], v[166:167], 1.0 op_sel_hi:[1,0]
	v_pk_mul_f32 v[186:187], v[10:11], v[186:187]
	v_pk_add_f32 v[216:217], v[164:165], 1.0 op_sel_hi:[1,0]
	v_pk_fma_f32 v[210:211], v[210:211], v[184:185], v[170:171]
	v_pk_mul_f32 v[184:185], v[222:223], v[220:221] op_sel_hi:[1,0]
	v_mov_b32_e32 v218, v221
	v_pk_fma_f32 v[216:217], v[216:217], v[186:187], v[168:169]
	v_pk_mul_f32 v[186:187], v[218:219], v[220:221] op_sel_hi:[1,0]
	v_pk_mul_f32 v[218:219], v[16:17], v[184:185]
	v_pk_add_f32 v[184:185], v[174:175], 1.0 op_sel_hi:[1,0]
	v_pk_mul_f32 v[220:221], v[14:15], v[186:187]
	v_pk_add_f32 v[186:187], v[172:173], 1.0 op_sel_hi:[1,0]
	v_pk_fma_f32 v[218:219], v[184:185], v[218:219], v[178:179]
	v_max_f32_e64 v184, |v208|, |v209|
	v_max_f32_e64 v185, |v206|, |v207|
	v_pk_fma_f32 v[220:221], v[186:187], v[220:221], v[176:177]
	v_max3_f32 v184, v184, 0, v185
	v_max_f32_e64 v185, |v214|, |v215|
	v_max_f32_e64 v186, |v212|, |v213|
	v_max3_f32 v184, v184, v185, v186
	v_max_f32_e64 v185, |v216|, |v217|
	v_max_f32_e64 v186, |v210|, |v211|
	v_max3_f32 v184, v184, v185, v186
	v_max_f32_e64 v185, |v220|, |v221|
	v_max_f32_e64 v186, |v218|, |v219|
	v_max3_f32 v184, v184, v185, v186
	ds_bpermute_b32 v185, v1, v184
	s_waitcnt lgkmcnt(0)
	v_max_f32_e32 v185, v185, v185
	v_max_f32_e32 v184, v184, v185
	ds_bpermute_b32 v185, v181, v184
	s_waitcnt lgkmcnt(0)
	v_max_f32_e32 v185, v185, v185
	v_max_f32_e32 v184, v184, v185
	ds_bpermute_b32 v185, v183, v184
	s_waitcnt lgkmcnt(0)
	v_max_f32_e32 v185, v185, v185
	v_max_f32_e32 v184, v184, v185
	ds_bpermute_b32 v185, v224, v184
	s_waitcnt lgkmcnt(0)
	v_max_f32_e32 v185, v185, v185
	v_max_f32_e32 v184, v184, v185
	ds_bpermute_b32 v185, v225, v184
	s_waitcnt lgkmcnt(0)
	v_max_f32_e32 v185, v185, v185
	v_max_f32_e32 v184, v184, v185
	ds_bpermute_b32 v185, v226, v184
	s_waitcnt lgkmcnt(0)
	v_max_f32_e32 v185, v185, v185
	v_max_f32_e32 v222, v184, v185
	v_div_scale_f32 v184, s[2:3], v222, v222, s10
	v_rcp_f32_e32 v185, v184
	v_cmp_lt_f32_e64 s[0:1], 0, v222
	v_fma_f32 v186, -v184, v185, 1.0
	v_fmac_f32_e32 v185, v186, v185
	v_div_scale_f32 v186, vcc, s10, v222, s10
	v_mul_f32_e32 v187, v186, v185
	v_fma_f32 v223, -v184, v187, v186
	v_fmac_f32_e32 v187, v223, v185
	v_fma_f32 v184, -v184, v187, v186
	v_div_fmas_f32 v184, v184, v185, v187
	v_div_fixup_f32 v184, v184, v222, s10
	v_cndmask_b32_e64 v184, 0, v184, s[0:1]
	v_mul_f32_e32 v186, v209, v184
	v_mul_f32_e32 v185, v208, v184
	v_rndne_f32_e32 v186, v186
	v_mul_f32_e32 v187, v206, v184
	v_mul_f32_e32 v223, v207, v184
	v_rndne_f32_e32 v185, v185
	v_cvt_i32_f32_e32 v186, v186
	v_rndne_f32_e32 v187, v187
	v_rndne_f32_e32 v223, v223
	v_cvt_i32_f32_e32 v185, v185
	v_cvt_i32_f32_sdwa v187, v187 dst_sel:WORD_1 dst_unused:UNUSED_PAD src0_sel:DWORD
	v_cvt_i32_f32_e32 v223, v223
	v_lshlrev_b32_e32 v186, 8, v186
	s_mov_b32 s0, 0x40c0c00
	v_and_b32_e32 v186, 0xff00, v186
	v_and_b32_e32 v187, 0xff0000, v187
	v_perm_b32 v185, v223, v185, s0
	v_or3_b32 v185, v185, v186, v187
	v_mul_f32_e32 v186, v215, v184
	global_store_dword v[194:195], v185, off offset:-512
	v_mul_f32_e32 v185, v214, v184
	v_rndne_f32_e32 v186, v186
	v_mul_f32_e32 v187, v212, v184
	v_mul_f32_e32 v223, v213, v184
	v_rndne_f32_e32 v185, v185
	v_cvt_i32_f32_e32 v186, v186
	v_rndne_f32_e32 v187, v187
	v_rndne_f32_e32 v223, v223
	v_cvt_i32_f32_e32 v185, v185
	v_cvt_i32_f32_sdwa v187, v187 dst_sel:WORD_1 dst_unused:UNUSED_PAD src0_sel:DWORD
	v_cvt_i32_f32_e32 v223, v223
	v_lshlrev_b32_e32 v186, 8, v186
	v_and_b32_e32 v186, 0xff00, v186
	v_and_b32_e32 v187, 0xff0000, v187
	v_perm_b32 v185, v223, v185, s0
	v_or3_b32 v185, v185, v186, v187
	v_mul_f32_e32 v186, v217, v184
	global_store_dword v[194:195], v185, off offset:-256
	v_mul_f32_e32 v185, v216, v184
	v_rndne_f32_e32 v186, v186
	v_mul_f32_e32 v187, v210, v184
	v_mul_f32_e32 v223, v211, v184
	v_rndne_f32_e32 v185, v185
	v_cvt_i32_f32_e32 v186, v186
	v_rndne_f32_e32 v187, v187
	v_rndne_f32_e32 v223, v223
	v_cvt_i32_f32_e32 v185, v185
	v_cvt_i32_f32_sdwa v187, v187 dst_sel:WORD_1 dst_unused:UNUSED_PAD src0_sel:DWORD
	v_cvt_i32_f32_e32 v223, v223
	v_lshlrev_b32_e32 v186, 8, v186
	v_and_b32_e32 v186, 0xff00, v186
	v_and_b32_e32 v187, 0xff0000, v187
	v_perm_b32 v185, v223, v185, s0
	v_or3_b32 v185, v185, v186, v187
	v_mul_f32_e32 v186, v221, v184
	global_store_dword v[194:195], v185, off
	v_mul_f32_e32 v185, v220, v184
	v_rndne_f32_e32 v186, v186
	v_mul_f32_e32 v187, v218, v184
	v_mul_f32_e32 v184, v219, v184
	v_rndne_f32_e32 v185, v185
	v_cvt_i32_f32_e32 v186, v186
	v_rndne_f32_e32 v187, v187
	v_rndne_f32_e32 v184, v184
	v_cvt_i32_f32_e32 v185, v185
	v_cvt_i32_f32_sdwa v187, v187 dst_sel:WORD_1 dst_unused:UNUSED_PAD src0_sel:DWORD
	v_cvt_i32_f32_e32 v184, v184
	v_lshlrev_b32_e32 v186, 8, v186
	v_and_b32_e32 v186, 0xff00, v186
	v_and_b32_e32 v187, 0xff0000, v187
	v_perm_b32 v184, v184, v185, s0
	v_or3_b32 v184, v184, v186, v187
	global_store_dword v[194:195], v184, off offset:256
	s_and_saveexec_b64 s[0:1], s[36:37]
	s_cbranch_execz .LBB0_1219
	v_mul_f32_e32 v184, 0x3c010204, v222
	global_store_dword v[204:205], v184, off

.LBB0_1630:
	v_readlane_b32 s40, v251, 5
	v_readlane_b32 s46, v251, 11
	v_readlane_b32 s47, v251, 12
	s_mov_b32 s0, 0xf800000
	s_mov_b32 s3, 0x42fe0000
	v_lshl_add_u64 v[62:63], s[46:47], 0, v[52:53]
	v_add_co_u32_e32 v62, vcc, 0x500000, v62
	v_readlane_b32 s41, v251, 6
	s_nop 0
	v_addc_co_u32_e32 v63, vcc, 0, v63, vcc
	global_load_dwordx2 v[64:65], v[62:63], off
	global_load_dwordx2 v[70:71], v[62:63], off offset:512
	global_load_dwordx2 v[76:77], v[62:63], off offset:1024
	s_nop 0
	global_load_dwordx2 v[62:63], v[62:63], off offset:1536
	v_readlane_b32 s42, v251, 7
	v_readlane_b32 s43, v251, 8
	v_readlane_b32 s44, v251, 9
	v_readlane_b32 s45, v251, 10
	s_waitcnt vmcnt(3)
	v_and_b32_e32 v89, 0xffff0000, v65
	v_and_b32_e32 v79, 0xffff0000, v64
	v_lshlrev_b32_e32 v88, 16, v65
	s_waitcnt vmcnt(0)
	v_lshlrev_b32_e32 v75, 16, v62
	v_and_b32_e32 v73, 0xffff0000, v62
	v_mul_f32_e32 v62, v89, v89
	v_lshlrev_b32_e32 v69, 16, v71
	v_lshlrev_b32_e32 v68, 16, v70
	v_and_b32_e32 v71, 0xffff0000, v71
	v_and_b32_e32 v70, 0xffff0000, v70
	v_lshlrev_b32_e32 v80, 16, v63
	v_and_b32_e32 v81, 0xffff0000, v63
	v_lshlrev_b32_e32 v78, 16, v64
	v_pk_fma_f32 v[90:91], v[88:89], v[88:89], v[62:63] op_sel_hi:[1,1,0]
	v_pk_mul_f32 v[62:63], v[70:71], v[70:71]
	v_mul_f32_e32 v72, v79, v79
	v_pk_fma_f32 v[92:93], v[68:69], v[68:69], v[62:63]
	v_lshlrev_b32_e32 v62, 16, v76
	v_and_b32_e32 v63, 0xffff0000, v76
	v_lshlrev_b32_e32 v64, 16, v77
	v_and_b32_e32 v65, 0xffff0000, v77
	v_pk_fma_f32 v[76:77], v[78:79], v[78:79], v[72:73] op_sel_hi:[1,1,0]
	v_mov_b32_e32 v94, v90
	v_mov_b32_e32 v74, v76
	v_mov_b32_e32 v95, v75
	v_pk_add_f32 v[76:77], v[76:77], v[90:91]
	v_pk_mul_f32 v[90:91], v[74:75], v[94:95]
	v_mul_f32_e32 v87, v73, v73
	v_mov_b32_e32 v77, v91
	v_pk_add_f32 v[90:91], v[92:93], v[92:93] op_sel:[0,1] op_sel_hi:[1,0]
	v_mul_f32_e32 v72, v63, v63
	v_mov_b32_e32 v91, v87
	v_pk_add_f32 v[76:77], v[76:77], v[90:91]
	v_pk_fma_f32 v[90:91], v[62:63], v[62:63], v[72:73] op_sel_hi:[1,1,0]
	v_mul_f32_e32 v72, v65, v65
	v_mul_f32_e32 v96, v80, v80
	v_mul_f32_e32 v97, v81, v81
	v_pk_fma_f32 v[92:93], v[64:65], v[64:65], v[72:73] op_sel_hi:[1,1,0]
	v_mov_b32_e32 v91, v96
	v_mov_b32_e32 v93, v97
	v_pk_add_f32 v[90:91], v[90:91], v[92:93]
	s_nop 0
	v_pk_add_f32 v[76:77], v[76:77], v[90:91]
	s_nop 0
	v_add_f32_e32 v72, v76, v77
	s_waitcnt lgkmcnt(0)
	s_nop 1
	v_add_f32_dpp v72, v72, v72 quad_perm:[1,0,3,2] row_mask:0xf bank_mask:0xf
	s_nop 1
	v_add_f32_dpp v72, v72, v72 quad_perm:[2,3,0,1] row_mask:0xf bank_mask:0xf
	s_nop 1
	v_add_f32_dpp v72, v72, v72 row_half_mirror row_mask:0xf bank_mask:0xf
	s_nop 1
	v_add_f32_dpp v72, v72, v72 row_mirror row_mask:0xf bank_mask:0xf
	s_nop 1
	v_readlane_b32 s98, v72, 0
	v_readlane_b32 s99, v72, 16
	v_readlane_b32 s100, v72, 32
	v_readlane_b32 s101, v72, 48
	s_nop 1
	v_mov_b32_e32 v74, s99
	v_add_f32_e32 v74, s98, v74
	v_mov_b32_e32 v72, s101
	v_add_f32_e32 v72, s100, v72
	v_add_f32_e32 v72, v74, v72
	v_fmamk_f32 v72, v72, 0x3a800000, v241
	v_cmp_gt_f32_e32 vcc, s0, v72
	v_mul_f32_e32 v74, 0x4f800000, v72
	s_nop 0
	v_cndmask_b32_e32 v72, v72, v74, vcc
	v_sqrt_f32_e32 v74, v72
	s_nop 0
	v_add_u32_e32 v76, -1, v74
	v_fma_f32 v77, -v76, v74, v72
	v_cmp_ge_f32_e64 s[0:1], 0, v77
	v_add_u32_e32 v77, 1, v74
	s_nop 0
	v_cndmask_b32_e64 v76, v74, v76, s[0:1]
	v_fma_f32 v74, -v77, v74, v72
	v_cmp_lt_f32_e64 s[0:1], 0, v74
	s_nop 1
	v_cndmask_b32_e64 v74, v76, v77, s[0:1]
	v_mul_f32_e32 v76, 0x37800000, v74
	v_cndmask_b32_e32 v74, v74, v76, vcc
	v_cmp_class_f32_e32 vcc, v72, v188
	s_nop 1
	v_cndmask_b32_e32 v72, v74, v72, vcc
	v_div_scale_f32 v74, s[0:1], v72, v72, 1.0
	v_rcp_f32_e32 v76, v74
	s_nop 0
	v_fma_f32 v77, -v74, v76, 1.0
	v_fmac_f32_e32 v76, v77, v76
	v_div_scale_f32 v77, vcc, 1.0, v72, 1.0
	v_mul_f32_e32 v87, v77, v76
	v_fma_f32 v90, -v74, v87, v77
	v_fmac_f32_e32 v87, v90, v76
	v_fma_f32 v74, -v74, v87, v77
	v_div_fmas_f32 v74, v74, v76, v87
	v_div_fixup_f32 v74, v74, v72, 1.0
	v_pk_mul_f32 v[76:77], v[74:75], v[88:89] op_sel_hi:[0,1]
	v_pk_mul_f32 v[76:77], v[4:5], v[76:77]
	v_pk_add_f32 v[88:89], v[20:21], 1.0 op_sel_hi:[1,0]
	v_pk_mul_f32 v[78:79], v[74:75], v[78:79] op_sel_hi:[0,1]
	v_pk_fma_f32 v[76:77], v[88:89], v[76:77], v[40:41]
	v_mov_b32_e32 v88, v69
	v_mov_b32_e32 v89, v71
	v_mov_b32_e32 v69, v70
	v_mov_b32_e32 v72, v75
	v_pk_mul_f32 v[78:79], v[2:3], v[78:79]
	v_pk_add_f32 v[90:91], v[18:19], 1.0 op_sel_hi:[1,0]
	v_pk_mul_f32 v[88:89], v[74:75], v[88:89] op_sel_hi:[0,1]
	v_pk_mul_f32 v[68:69], v[74:75], v[68:69] op_sel_hi:[0,1]
	v_pk_mul_f32 v[80:81], v[80:81], v[74:75] op_sel_hi:[1,0]
	v_pk_mul_f32 v[72:73], v[72:73], v[74:75] op_sel_hi:[1,0]
	v_pk_fma_f32 v[78:79], v[90:91], v[78:79], v[38:39]
	v_pk_mul_f32 v[70:71], v[6:7], v[68:69]
	v_pk_mul_f32 v[68:69], v[8:9], v[88:89]
	v_pk_add_f32 v[88:89], v[24:25], 1.0 op_sel_hi:[1,0]
	v_pk_add_f32 v[90:91], v[22:23], 1.0 op_sel_hi:[1,0]
	v_pk_mul_f32 v[64:65], v[74:75], v[64:65] op_sel_hi:[0,1]
	v_pk_mul_f32 v[62:63], v[74:75], v[62:63] op_sel_hi:[0,1]
	v_pk_mul_f32 v[74:75], v[14:15], v[72:73]
	v_pk_mul_f32 v[72:73], v[16:17], v[80:81]
	v_pk_add_f32 v[80:81], v[32:33], 1.0 op_sel_hi:[1,0]
	v_pk_fma_f32 v[68:69], v[88:89], v[68:69], v[28:29]
	v_pk_fma_f32 v[70:71], v[90:91], v[70:71], v[26:27]
	v_pk_mul_f32 v[88:89], v[10:11], v[62:63]
	v_pk_mul_f32 v[62:63], v[12:13], v[64:65]
	v_pk_add_f32 v[64:65], v[36:37], 1.0 op_sel_hi:[1,0]
	v_pk_add_f32 v[90:91], v[34:35], 1.0 op_sel_hi:[1,0]
	v_pk_fma_f32 v[72:73], v[80:81], v[72:73], v[48:49]
	v_max_f32_e64 v80, |v78|, |v79|
	v_max_f32_e64 v81, |v76|, |v77|
	v_pk_fma_f32 v[62:63], v[64:65], v[62:63], v[44:45]
	v_pk_fma_f32 v[64:65], v[90:91], v[88:89], v[42:43]
	v_pk_add_f32 v[88:89], v[30:31], 1.0 op_sel_hi:[1,0]
	v_max3_f32 v80, v80, 0, v81
	v_max_f32_e64 v81, |v70|, |v71|
	v_max_f32_e64 v87, |v68|, |v69|
	v_pk_fma_f32 v[74:75], v[88:89], v[74:75], v[46:47]
	v_max3_f32 v80, v80, v81, v87
	v_max_f32_e64 v81, |v64|, |v65|
	v_max_f32_e64 v87, |v62|, |v63|
	v_max3_f32 v80, v80, v81, v87
	v_max_f32_e64 v81, |v74|, |v75|
	v_max_f32_e64 v87, |v72|, |v73|
	v_max3_f32 v80, v80, v81, v87
	s_waitcnt lgkmcnt(0)
	s_nop 1
	v_max_f32_dpp v80, v80, v80 quad_perm:[1,0,3,2] row_mask:0xf bank_mask:0xf
	s_nop 1
	v_max_f32_dpp v80, v80, v80 quad_perm:[2,3,0,1] row_mask:0xf bank_mask:0xf
	s_nop 1
	v_max_f32_dpp v80, v80, v80 row_half_mirror row_mask:0xf bank_mask:0xf
	s_nop 1
	v_max_f32_dpp v80, v80, v80 row_mirror row_mask:0xf bank_mask:0xf
	s_nop 1
	v_readlane_b32 s98, v80, 0
	v_readlane_b32 s99, v80, 16
	v_readlane_b32 s100, v80, 32
	v_readlane_b32 s101, v80, 48
	s_nop 1
	v_mov_b32_e32 v81, s99
	v_max_f32_e32 v81, s98, v81
	v_mov_b32_e32 v80, s101
	v_max_f32_e32 v80, s100, v80
	v_max_f32_e32 v80, v81, v80
	v_div_scale_f32 v81, s[10:11], v80, v80, s3
	v_rcp_f32_e32 v87, v81
	v_cmp_lt_f32_e64 s[0:1], 0, v80
	v_fma_f32 v88, -v81, v87, 1.0
	v_fmac_f32_e32 v87, v88, v87
	v_div_scale_f32 v88, vcc, s3, v80, s3
	v_mul_f32_e32 v89, v88, v87
	v_fma_f32 v90, -v81, v89, v88
	v_fmac_f32_e32 v89, v90, v87
	v_fma_f32 v81, -v81, v89, v88
	v_div_fmas_f32 v81, v81, v87, v89
	v_div_fixup_f32 v81, v81, v80, s3
	v_cndmask_b32_e64 v81, 0, v81, s[0:1]
	v_mul_f32_e32 v79, v79, v81
	v_mul_f32_e32 v78, v78, v81
	v_rndne_f32_e32 v79, v79
	v_mul_f32_e32 v76, v76, v81
	v_mul_f32_e32 v77, v77, v81
	v_mul_f32_e32 v65, v65, v81
	v_rndne_f32_e32 v78, v78
	v_cvt_i32_f32_e32 v79, v79
	v_rndne_f32_e32 v76, v76
	v_rndne_f32_e32 v77, v77
	v_mul_f32_e32 v64, v64, v81
	v_rndne_f32_e32 v65, v65
	v_mul_f32_e32 v62, v62, v81
	v_mul_f32_e32 v63, v63, v81
	v_cvt_i32_f32_e32 v78, v78
	v_cvt_i32_f32_sdwa v76, v76 dst_sel:WORD_1 dst_unused:UNUSED_PAD src0_sel:DWORD
	v_cvt_i32_f32_e32 v77, v77
	v_rndne_f32_e32 v64, v64
	v_cvt_i32_f32_e32 v65, v65
	v_rndne_f32_e32 v62, v62
	v_rndne_f32_e32 v63, v63
	v_cvt_i32_f32_e32 v64, v64
	v_cvt_i32_f32_sdwa v62, v62 dst_sel:WORD_1 dst_unused:UNUSED_PAD src0_sel:DWORD
	v_cvt_i32_f32_e32 v63, v63
	v_lshlrev_b32_e32 v79, 8, v79
	s_mov_b32 s0, 0x40c0c00
	v_lshl_add_u64 v[88:89], s[46:47], 0, v[56:57]
	v_and_b32_e32 v79, 0xff00, v79
	v_and_b32_e32 v76, 0xff0000, v76
	v_perm_b32 v77, v77, v78, s0
	s_mov_b32 s1, 0x8900000
	v_lshlrev_b32_e32 v65, 8, v65
	v_or3_b32 v78, v77, v79, v76
	v_add_co_u32_e32 v76, vcc, s1, v88
	v_and_b32_e32 v65, 0xff00, v65
	v_and_b32_e32 v62, 0xff0000, v62
	v_perm_b32 v63, v63, v64, s0
	v_addc_co_u32_e32 v77, vcc, 0, v89, vcc
	v_mul_f32_e32 v71, v71, v81
	v_or3_b32 v62, v63, v65, v62
	v_mul_f32_e32 v63, v75, v81
	v_mul_f32_e32 v70, v70, v81
	v_rndne_f32_e32 v71, v71
	v_mul_f32_e32 v68, v68, v81
	v_mul_f32_e32 v69, v69, v81
	global_store_dword v[76:77], v62, off offset:512
	v_mul_f32_e32 v62, v74, v81
	v_rndne_f32_e32 v63, v63
	v_mul_f32_e32 v64, v72, v81
	v_mul_f32_e32 v65, v73, v81
	v_rndne_f32_e32 v70, v70
	v_cvt_i32_f32_e32 v71, v71
	v_rndne_f32_e32 v68, v68
	v_rndne_f32_e32 v69, v69
	v_rndne_f32_e32 v62, v62
	v_cvt_i32_f32_e32 v63, v63
	v_rndne_f32_e32 v64, v64
	v_rndne_f32_e32 v65, v65
	v_cvt_i32_f32_e32 v70, v70
	v_cvt_i32_f32_sdwa v68, v68 dst_sel:WORD_1 dst_unused:UNUSED_PAD src0_sel:DWORD
	v_cvt_i32_f32_e32 v69, v69
	v_cvt_i32_f32_e32 v62, v62
	v_cvt_i32_f32_sdwa v64, v64 dst_sel:WORD_1 dst_unused:UNUSED_PAD src0_sel:DWORD
	v_cvt_i32_f32_e32 v65, v65
	v_lshlrev_b32_e32 v71, 8, v71
	v_lshlrev_b32_e32 v63, 8, v63
	v_and_b32_e32 v71, 0xff00, v71
	v_and_b32_e32 v68, 0xff0000, v68
	v_perm_b32 v69, v69, v70, s0
	v_and_b32_e32 v63, 0xff00, v63
	v_and_b32_e32 v64, 0xff0000, v64
	v_perm_b32 v62, v65, v62, s0
	v_or3_b32 v68, v69, v71, v68
	v_or3_b32 v62, v62, v63, v64
	global_store_dword v[76:77], v78, off
	global_store_dword v[76:77], v68, off offset:256
	global_store_dword v[76:77], v62, off offset:768
	s_and_saveexec_b64 s[0:1], s[36:37]
	s_cbranch_execz .LBB0_1627
	v_readlane_b32 s40, v251, 5
	v_readlane_b32 s46, v251, 11
	v_readlane_b32 s47, v251, 12
	v_mul_f32_e32 v64, 0x3c010204, v80
	v_readlane_b32 s41, v251, 6
	v_lshl_add_u64 v[62:63], s[46:47], 0, v[60:61]
	v_readlane_b32 s42, v251, 7
	v_readlane_b32 s43, v251, 8
	v_readlane_b32 s44, v251, 9
	v_readlane_b32 s45, v251, 10
	global_store_dword v[62:63], v64, off
	s_branch .LBB0_1627
